# merge-GEMM phase gets staggered conversion slots in both layers (4096 more items out of the prologue, which keeps 4608); FFN-up layer-0 slots now convert layer-0 down-proj weights
# baseline (speedup 1.0000x reference)
.LBB0_41:
	v_writelane_b32 v253, s24, 32
	v_writelane_b32 v253, s23, 34
	v_writelane_b32 v253, s22, 36
	s_mov_b32 s3, 0
	v_readlane_b32 s0, v253, 29
	s_lshl_b32 s0, s0, 14
	s_add_i32 s29, s0, 0
	s_cmp_lg_u64 s[48:49], 0
	v_readlane_b32 s4, v253, 30
	s_cselect_b64 s[44:45], -1, 0
	s_abs_i32 s2, s4
	v_cvt_f32_u32_e32 v2, s2
	s_sub_i32 s0, 0, s2
	s_ashr_i32 s6, s4, 31
	v_rcp_iflag_f32_e32 v2, v2
	s_nop 0
	v_mul_f32_e32 v2, 0x4f7ffffe, v2
	v_cvt_u32_f32_e32 v2, v2
	s_nop 0
	v_readfirstlane_b32 s1, v2
	s_mul_i32 s0, s0, s1
	s_mul_hi_u32 s0, s1, s0
	s_add_i32 s7, s1, s0
	s_mul_hi_u32 s0, s7, 0x4200
	s_mul_i32 s0, s0, s2
	s_sub_i32 s0, 0x4200, s0
	s_sub_i32 s1, s0, s2
	s_cmp_ge_u32 s0, s2
	s_cselect_b32 s0, s1, s0
	s_sub_i32 s1, s0, s2
	s_cmp_ge_u32 s0, s2
	s_cselect_b32 s8, s1, s0
	s_add_i32 s0, s4, 0xffffff00
	s_cmp_ge_i32 s0, s8
	s_cselect_b64 s[0:1], -1, 0
	s_cmpk_lt_u32 s8, 0x2101
	s_cselect_b64 s[4:5], -1, 0
	s_sub_i32 s8, 0x4200, s8
	s_and_b64 s[0:1], s[0:1], s[4:5]
	s_and_b64 s[0:1], s[0:1], exec
	s_cselect_b32 s5, s8, 0x4200
	s_add_i32 s0, s5, 0xffffd200
	s_cmp_eq_u32 s2, 0x800
	s_cselect_b32 s5, s0, s5
	v_writelane_b32 v253, s5, 38
	v_writelane_b32 v253, s48, 40
	s_mul_hi_u32 s0, s5, s7
	s_mul_i32 s1, s0, s2
	v_writelane_b32 v253, s49, 41
	v_writelane_b32 v253, s50, 42
	v_writelane_b32 v253, s51, 43
	v_writelane_b32 v253, s52, 44
	v_writelane_b32 v253, s53, 45
	v_writelane_b32 v253, s54, 46
	v_writelane_b32 v253, s55, 47
	s_sub_i32 s1, s5, s1
	v_writelane_b32 v253, s56, 48
	s_add_i32 s4, s0, 1
	s_sub_i32 s5, s1, s2
	v_writelane_b32 v253, s57, 49
	s_cmp_ge_u32 s1, s2
	v_writelane_b32 v253, s58, 50
	s_cselect_b32 s0, s4, s0
	v_writelane_b32 v253, s59, 51
	s_cselect_b32 s1, s5, s1
	s_add_i32 s4, s0, 1
	v_writelane_b32 v253, s60, 52
	s_cmp_ge_u32 s1, s2
	v_writelane_b32 v253, s61, 53
	s_cselect_b32 s0, s4, s0
	v_writelane_b32 v253, s62, 54
	s_xor_b32 s0, s0, s6
	v_writelane_b32 v253, s63, 55
	s_sub_i32 s15, s0, s6
	v_writelane_b32 v253, s29, 56
	s_add_i32 s14, s15, -1
	v_writelane_b32 v253, s44, 57
	s_cmp_lt_i32 s15, 1
	v_readfirstlane_b32 s0, v0
	v_writelane_b32 v253, s45, 58
	s_cbranch_scc1 .LBB0_65
	s_ashr_i32 s0, s0, 6
	s_min_i32 s18, s0, s14
	s_cmpk_gt_i32 s27, 0x7ff
	v_readlane_b32 s0, v253, 26
	s_cselect_b64 s[20:21], -1, 0
	s_add_u32 s0, s0, 0x800000
	v_writelane_b32 v253, s0, 59
	v_mov_b32_e32 v133, 0
	v_readlane_b32 s0, v253, 27
	s_addc_u32 s0, s0, 0
	s_add_i32 s25, 0, 0x21000
	v_writelane_b32 v253, s0, 61
	s_add_i32 s0, 0, 0x21200
	v_writelane_b32 v253, s0, 63
	s_add_i32 s0, 0, 0x21100
	v_writelane_b32 v254, s0, 1
	s_add_i32 s0, 0, 0x21300
	v_writelane_b32 v254, s0, 3
	v_writelane_b32 v254, s27, 5
	v_writelane_b32 v254, s14, 7
	v_writelane_b32 v254, s15, 9
	v_writelane_b32 v254, s18, 11
	v_writelane_b32 v254, s20, 13
	s_mov_b32 s22, 0x42800000
	s_mov_b32 s19, 0
	v_writelane_b32 v254, s21, 14
	s_branch .LBB0_45

.LBB0_557:
	s_or_b64 exec, exec, s[30:31]
	v_mov_b32_e32 v10, v0
	s_mov_b64 s[0:1], 0
	s_mov_b32 s24, s37
	v_readlane_b32 s25, v253, 8
	s_waitcnt lgkmcnt(0)
	s_barrier
	v_readlane_b32 s1, v253, 9
	s_cmpk_lg_i32 s1, 0x100
	s_cbranch_scc1 .Lfs5_skip
	s_cmpk_gt_i32 s25, 0x7f
	s_cbranch_scc1 .Lfs5_skip
	v_readlane_b32 s1, v254, 20
	s_movk_i32 s2, 0x2e00
	s_cmp_lg_u32 s1, 0
	s_cselect_b32 s2, 0x1600, s2
	v_readfirstlane_b32 s1, v0
	s_lshl_b32 s0, s25, 3
	s_lshr_b32 s1, s1, 6
	s_add_i32 s0, s0, s1
	s_add_i32 s0, s0, s2
	s_mov_b32 s101, 5
	v_readlane_b32 s62, v253, 54
	v_readlane_b32 s26, v253, 55
	s_mov_b32 s73, 0x10000
	v_mov_b32_e32 v135, v0
	v_and_b32_e32 v132, 63, v0
	s_branch .Ltkf_go

.Lfs5_skip:
	v_mov_b32_e32 v10, v0
	s_mov_b64 s[0:1], 0
	s_mov_b32 s24, s37
	v_readlane_b32 s25, v253, 8
	s_cmpk_lt_i32 s25, 0x200
	v_readfirstlane_b32 s4, v10
	s_cbranch_scc0 .LBB0_590
	s_ashr_i32 s26, s25, 31
	s_lshr_b32 s2, s26, 29
	s_add_i32 s7, s25, s2
	s_and_b32 s2, s7, -8
	s_sub_i32 s5, s25, s2
	s_cmp_gt_i32 s5, -1
	s_mov_b64 s[2:3], -1
	s_cbranch_scc0 .LBB0_560
	s_lshl_b32 s6, s5, 6
	s_mov_b64 s[2:3], 0

.LBB0_589:
	s_waitcnt vmcnt(0)
	v_readlane_b32 s37, v253, 9
	s_barrier
	v_readlane_b32 s1, v253, 9
	s_cmpk_lg_i32 s1, 0x100
	s_cbranch_scc1 .Lfs6_skip
	v_readlane_b32 s27, v253, 8
	s_cmpk_lt_i32 s27, 0x80
	s_cbranch_scc1 .Lfs6_skip
	v_readlane_b32 s1, v254, 20
	s_movk_i32 s2, 0x2600
	s_cmp_lg_u32 s1, 0
	s_cselect_b32 s2, 0xe00, s2
	v_readfirstlane_b32 s1, v0
	s_lshl_b32 s0, s27, 3
	s_lshr_b32 s1, s1, 6
	s_add_i32 s0, s0, s1
	s_add_i32 s0, s0, s2
	s_mov_b32 s101, 6
	v_readlane_b32 s62, v253, 54
	v_readlane_b32 s26, v253, 55
	s_mov_b32 s73, 0x10000
	v_mov_b32_e32 v135, v0
	v_and_b32_e32 v132, 63, v0
	s_branch .Ltkf_go

.Lfs6_skip:
.LBB0_590:
	s_getreg_b32 s0, hwreg(HW_REG_XCC_ID, 0, 4)
	s_waitcnt vmcnt(0)
	s_waitcnt lgkmcnt(0)
	s_barrier
	s_mov_b64 s[2:3], exec
	v_readlane_b32 s4, v253, 4
	v_readlane_b32 s5, v253, 5
	s_and_b64 s[4:5], s[2:3], s[4:5]
	s_xor_b64 s[30:31], s[4:5], s[2:3]
	s_mov_b64 exec, s[4:5]
	s_cbranch_execz .LBB0_644
	v_readlane_b32 s1, v254, 24
	s_waitcnt vmcnt(0) expcnt(0) lgkmcnt(0)
	s_and_b32 s37, s0, 15
	v_mov_b32_e32 v2, s1
	ds_read_b32 v4, v2
	v_readlane_b32 s1, v254, 17
	s_waitcnt lgkmcnt(0)
	v_cmp_ne_u32_e32 vcc, 0, v4
	v_mov_b32_e32 v2, s1
	ds_read_b32 v2, v2
	s_cbranch_vccnz .LBB0_607
	v_readlane_b32 s2, v253, 0
	v_readlane_b32 s3, v253, 1
	s_load_dwordx2 s[0:1], s[2:3], 0x4
	v_readlane_b32 s2, v253, 9
	s_mov_b32 s16, 1
	s_waitcnt lgkmcnt(0)
	s_mul_i32 s17, s0, s2
	s_mul_i32 s17, s17, s1
	s_mov_b64 s[0:1], 0
	s_branch .LBB0_595

.LBB0_893:
	s_cmp_eq_u32 s101, 0
	s_cbranch_scc1 .Lfret_none
	s_cmp_eq_u32 s101, 1
	s_cbranch_scc1 .Lfret_1
	s_cmp_eq_u32 s101, 2
	s_cbranch_scc1 .Lfret_2
	s_cmp_eq_u32 s101, 3
	s_cbranch_scc1 .Lfret_3
	s_cmp_eq_u32 s101, 4
	s_cbranch_scc1 .Lfret_4
	s_cmp_eq_u32 s101, 5
	s_cbranch_scc1 .Lfret_5
	s_branch .Lfret_6

.LBB0_947:
	s_or_b64 exec, exec, s[30:31]
	v_mov_b32_e32 v6, v0
	s_mov_b64 s[0:1], 0
	v_readlane_b32 s36, v253, 8
	s_waitcnt lgkmcnt(0)
	s_barrier
	v_readlane_b32 s1, v253, 9
	s_cmpk_lg_i32 s1, 0x100
	s_cbranch_scc1 .Lfs1_skip
	v_readlane_b32 s1, v254, 20
	s_cmp_eq_u32 s1, 0
	s_cbranch_scc1 .Lfs1_skip
	s_cmpk_gt_i32 s36, 0x7f
	s_cbranch_scc1 .Lfs1_skip
	v_readfirstlane_b32 s1, v0
	s_lshl_b32 s0, s36, 3
	s_lshr_b32 s1, s1, 6
	s_add_i32 s0, s0, s1
	s_addk_i32 s0, 0x1e00
	s_mov_b32 s101, 1
	v_readlane_b32 s62, v253, 54
	v_readlane_b32 s26, v253, 55
	s_mov_b32 s73, 0x10000
	v_mov_b32_e32 v135, v0
	v_and_b32_e32 v132, 63, v0
	s_branch .Ltkf_go

.LBB0_971:
	s_waitcnt vmcnt(0)
	s_barrier
	v_readlane_b32 s1, v253, 9
	s_cmpk_lg_i32 s1, 0x100
	s_cbranch_scc1 .Lfs2_skip
	v_readlane_b32 s1, v254, 20
	s_cmp_eq_u32 s1, 0
	s_cbranch_scc1 .Lfs2_skip
	v_readlane_b32 s27, v253, 8
	s_cmpk_lt_i32 s27, 0x80
	s_cbranch_scc1 .Lfs2_skip
	v_readfirstlane_b32 s1, v0
	s_lshl_b32 s0, s27, 3
	s_lshr_b32 s1, s1, 6
	s_add_i32 s0, s0, s1
	s_addk_i32 s0, 0x1600
	s_mov_b32 s101, 2
	v_readlane_b32 s62, v253, 54
	v_readlane_b32 s26, v253, 55
	s_mov_b32 s73, 0x10000
	v_mov_b32_e32 v135, v0
	v_and_b32_e32 v132, 63, v0
	s_branch .Ltkf_go
